# lever 8, second form: mixer-A bias-table reads of head k+1 issued in the s_nop padding behind head k's QK MFMAs
# baseline (speedup 1.0000x reference)
.LBB0_806:
	s_min_u32 s8, s7, 8
	s_add_i32 s8, s8, s6
	v_med3_i32 v5, s8, 0, v184
	v_lshl_or_b32 v2, v5, 11, v160
	v_lshl_add_u64 v[94:95], v[172:173], 0, v[2:3]
	v_lshlrev_b32_e32 v2, 12, v5
	v_lshl_add_u64 v[122:123], v[174:175], 0, v[2:3]
	global_load_dwordx4 v[90:93], v[94:95], off
	s_nop 0
	global_load_dwordx4 v[94:97], v[94:95], off offset:1024
	s_nop 0
	global_load_dwordx4 v[106:109], v[122:123], off
	global_load_dwordx4 v[110:113], v[122:123], off offset:1024
	global_load_dwordx4 v[118:121], v[122:123], off offset:2048
	s_nop 0
	global_load_dwordx4 v[122:125], v[122:123], off offset:3072
	s_add_i32 s8, s6, s7
	s_add_i32 s8, s8, -1
	s_cmpk_gt_u32 s8, 0xff
	s_cbranch_scc1 .LBB0_816
	ds_read2_b32 v[134:135], v190 offset1:1
	ds_read2_b32 v[136:137], v190 offset0:2 offset1:3
	ds_read2_b32 v[192:193], v190 offset0:16 offset1:17
	ds_read2_b32 v[194:195], v190 offset0:18 offset1:19
	s_waitcnt vmcnt(11) lgkmcnt(2)
	v_mfma_f32_16x16x32_fp8_fp8 v[134:137], v[130:131], v[70:71], v[134:137]
	v_mfma_f32_16x16x32_fp8_fp8 v[138:141], v[132:133], v[72:73], v[134:137]
	s_waitcnt vmcnt(10) lgkmcnt(0)
	v_mfma_f32_16x16x32_fp8_fp8 v[134:137], v[126:127], v[70:71], v[192:195]
	v_mfma_f32_16x16x32_fp8_fp8 v[134:137], v[128:129], v[72:73], v[134:137]
	v_add_u32_e32 v246, 0x504, v190
	v_add_u32_e32 v247, 0x50c, v190
	ds_read2_b32 v[222:223], v246 offset1:1
	ds_read2_b32 v[224:225], v247 offset1:1
	v_add_u32_e32 v246, 0x544, v190
	v_add_u32_e32 v247, 0x54c, v190
	ds_read2_b32 v[226:227], v246 offset1:1
	ds_read2_b32 v[228:229], v247 offset1:1
	v_max_f32_e32 v2, v139, v139
	v_max_f32_e32 v5, v138, v138
	v_max_f32_e32 v2, v5, v2
	v_max_f32_e32 v5, v141, v141
	v_max_f32_e32 v191, v140, v140
	v_max_f32_e32 v5, v191, v5
	v_max_f32_e32 v191, v137, v137
	v_max_f32_e32 v192, v136, v136
	v_max_f32_e32 v191, v192, v191
	v_max3_f32 v191, v134, v135, v191
	v_max3_f32 v2, v2, v5, v191
	v_mov_b32_e32 v5, v2
	s_nop 1
	v_permlane16_swap_b32_e32 v2, v5
	v_max_f32_e32 v5, v5, v5
	v_max_f32_e32 v2, v2, v2
	v_max_f32_e32 v2, v2, v5
	v_mov_b32_e32 v5, v2
	s_nop 1
	v_permlane32_swap_b32_e32 v2, v5
	v_max_f32_e32 v5, v5, v5
	v_max_f32_e32 v2, v2, v2
	v_max_f32_e32 v2, v2, v5
	v_cmp_gt_f32_e32 vcc, v2, v176
	s_cbranch_vccz .LBB0_809
	v_max_f32_e32 v2, v2, v2
	v_max_f32_e32 v5, v176, v176
	v_max_f32_e32 v5, v5, v2
	v_sub_f32_e32 v2, v176, v5
	v_exp_f32_e32 v2, v2
	v_mov_b32_e32 v176, v5
	v_mul_f32_e32 v4, v4, v2
	v_pk_mul_f32 v[68:69], v[68:69], v[2:3] op_sel_hi:[1,0]
	v_pk_mul_f32 v[66:67], v[66:67], v[2:3] op_sel_hi:[1,0]
	v_pk_mul_f32 v[64:65], v[64:65], v[2:3] op_sel_hi:[1,0]
	v_pk_mul_f32 v[62:63], v[62:63], v[2:3] op_sel_hi:[1,0]
	v_pk_mul_f32 v[60:61], v[60:61], v[2:3] op_sel_hi:[1,0]
	v_pk_mul_f32 v[58:59], v[58:59], v[2:3] op_sel_hi:[1,0]
	v_pk_mul_f32 v[56:57], v[56:57], v[2:3] op_sel_hi:[1,0]
	v_pk_mul_f32 v[54:55], v[54:55], v[2:3] op_sel_hi:[1,0]
.LBB0_809:
	v_sub_f32_e32 v134, v134, v176
	v_exp_f32_e32 v193, v134
	v_sub_f32_e32 v134, v135, v176
	v_sub_f32_e32 v2, v138, v176
	v_sub_f32_e32 v138, v140, v176
	v_exp_f32_e32 v194, v134
	v_sub_f32_e32 v134, v136, v176
	v_sub_f32_e32 v5, v139, v176
	v_exp_f32_e32 v191, v138
	v_sub_f32_e32 v138, v141, v176
	v_exp_f32_e32 v195, v134
	v_sub_f32_e32 v134, v137, v176
	v_exp_f32_e32 v2, v2
	v_exp_f32_e32 v5, v5
	v_exp_f32_e32 v192, v138
	v_exp_f32_e32 v196, v134
	v_cvt_pk_bf16_f32 v136, v193, v194
	v_cvt_pk_bf16_f32 v134, v2, v5
	v_cvt_pk_bf16_f32 v135, v191, v192
	v_cvt_pk_bf16_f32 v137, v195, v196
	s_waitcnt vmcnt(9)
	s_nop 0
	v_mfma_f32_16x16x32_bf16 v[66:69], v[114:117], v[134:137], v[66:69]
	s_waitcnt vmcnt(8)
	v_mfma_f32_16x16x32_bf16 v[62:65], v[102:105], v[134:137], v[62:65]
	s_waitcnt vmcnt(7)
	v_mfma_f32_16x16x32_bf16 v[58:61], v[98:101], v[134:137], v[58:61]
	s_waitcnt vmcnt(6)
	v_mfma_f32_16x16x32_bf16 v[54:57], v[86:89], v[134:137], v[54:57]
	s_waitcnt lgkmcnt(0)
	v_mfma_f32_16x16x32_fp8_fp8 v[134:137], v[130:131], v[74:75], v[222:225]
	v_mfma_f32_16x16x32_fp8_fp8 v[138:141], v[132:133], v[76:77], v[134:137]
	v_mfma_f32_16x16x32_fp8_fp8 v[134:137], v[126:127], v[74:75], v[226:229]
	v_mfma_f32_16x16x32_fp8_fp8 v[134:137], v[128:129], v[76:77], v[134:137]
	v_add_u32_e32 v246, 0xa08, v190
	v_add_u32_e32 v247, 0xa10, v190
	ds_read2_b32 v[230:231], v246 offset1:1
	ds_read2_b32 v[232:233], v247 offset1:1
	v_add_u32_e32 v246, 0xa48, v190
	v_add_u32_e32 v247, 0xa50, v190
	ds_read2_b32 v[234:235], v246 offset1:1
	ds_read2_b32 v[236:237], v247 offset1:1
	v_max_f32_e32 v197, v139, v139
	v_max_f32_e32 v198, v138, v138
	v_max_f32_e32 v197, v198, v197
	v_max_f32_e32 v198, v141, v141
	v_max_f32_e32 v199, v140, v140
	v_max_f32_e32 v198, v199, v198
	v_max_f32_e32 v199, v137, v137
	v_max_f32_e32 v200, v136, v136
	v_max_f32_e32 v199, v200, v199
	v_max3_f32 v199, v134, v135, v199
	v_max3_f32 v197, v197, v198, v199
	v_mov_b32_e32 v198, v197
	s_nop 1
	v_permlane16_swap_b32_e32 v197, v198
	v_max_f32_e32 v198, v198, v198
	v_max_f32_e32 v197, v197, v197
	v_max_f32_e32 v197, v197, v198
	v_mov_b32_e32 v198, v197
	s_nop 1
	v_permlane32_swap_b32_e32 v197, v198
	v_max_f32_e32 v198, v198, v198
	v_max_f32_e32 v197, v197, v197
	v_max_f32_e32 v197, v197, v198
	v_cmp_gt_f32_e32 vcc, v197, v177
	s_cbranch_vccz .LBB0_811
	v_max_f32_e32 v197, v197, v197
	v_max_f32_e32 v198, v177, v177
	v_max_f32_e32 v197, v198, v197
	v_sub_f32_e32 v177, v177, v197
	v_exp_f32_e32 v198, v177
	v_mov_b32_e32 v177, v197
	v_mul_f32_e32 v189, v189, v198
	v_pk_mul_f32 v[52:53], v[52:53], v[198:199] op_sel_hi:[1,0]
	v_pk_mul_f32 v[50:51], v[50:51], v[198:199] op_sel_hi:[1,0]
	v_pk_mul_f32 v[48:49], v[48:49], v[198:199] op_sel_hi:[1,0]
	v_pk_mul_f32 v[46:47], v[46:47], v[198:199] op_sel_hi:[1,0]
	v_pk_mul_f32 v[44:45], v[44:45], v[198:199] op_sel_hi:[1,0]
	v_pk_mul_f32 v[42:43], v[42:43], v[198:199] op_sel_hi:[1,0]
	v_pk_mul_f32 v[40:41], v[40:41], v[198:199] op_sel_hi:[1,0]
	v_pk_mul_f32 v[38:39], v[38:39], v[198:199] op_sel_hi:[1,0]
.LBB0_811:
	v_sub_f32_e32 v138, v138, v177
	v_sub_f32_e32 v134, v134, v177
	v_exp_f32_e32 v197, v138
	v_sub_f32_e32 v138, v139, v177
	v_exp_f32_e32 v201, v134
	v_sub_f32_e32 v134, v135, v177
	v_exp_f32_e32 v198, v138
	v_sub_f32_e32 v138, v140, v177
	v_exp_f32_e32 v202, v134
	v_sub_f32_e32 v134, v136, v177
	v_exp_f32_e32 v199, v138
	v_sub_f32_e32 v138, v141, v177
	v_exp_f32_e32 v203, v134
	v_sub_f32_e32 v134, v137, v177
	v_exp_f32_e32 v200, v138
	v_exp_f32_e32 v204, v134
	v_cvt_pk_bf16_f32 v134, v197, v198
	v_cvt_pk_bf16_f32 v136, v201, v202
	v_cvt_pk_bf16_f32 v135, v199, v200
	v_cvt_pk_bf16_f32 v137, v203, v204
	s_nop 1
	v_mfma_f32_16x16x32_bf16 v[50:53], v[114:117], v[134:137], v[50:53]
	v_mfma_f32_16x16x32_bf16 v[46:49], v[102:105], v[134:137], v[46:49]
	v_mfma_f32_16x16x32_bf16 v[42:45], v[98:101], v[134:137], v[42:45]
	v_mfma_f32_16x16x32_bf16 v[38:41], v[86:89], v[134:137], v[38:41]
	s_waitcnt lgkmcnt(0)
	v_mfma_f32_16x16x32_fp8_fp8 v[134:137], v[130:131], v[78:79], v[230:233]
	v_mfma_f32_16x16x32_fp8_fp8 v[138:141], v[132:133], v[80:81], v[134:137]
	v_mfma_f32_16x16x32_fp8_fp8 v[134:137], v[126:127], v[78:79], v[234:237]
	v_mfma_f32_16x16x32_fp8_fp8 v[134:137], v[128:129], v[80:81], v[134:137]
	v_add_u32_e32 v246, 0xf0c, v190
	v_add_u32_e32 v247, 0xf14, v190
	ds_read2_b32 v[238:239], v246 offset1:1
	ds_read2_b32 v[240:241], v247 offset1:1
	v_add_u32_e32 v246, 0xf4c, v190
	v_add_u32_e32 v247, 0xf54, v190
	ds_read2_b32 v[242:243], v246 offset1:1
	ds_read2_b32 v[244:245], v247 offset1:1
	v_max_f32_e32 v205, v139, v139
	v_max_f32_e32 v206, v138, v138
	v_max_f32_e32 v205, v206, v205
	v_max_f32_e32 v206, v141, v141
	v_max_f32_e32 v207, v140, v140
	v_max_f32_e32 v206, v207, v206
	v_max_f32_e32 v207, v137, v137
	v_max_f32_e32 v208, v136, v136
	v_max_f32_e32 v207, v208, v207
	v_max3_f32 v207, v134, v135, v207
	v_max3_f32 v205, v205, v206, v207
	v_mov_b32_e32 v206, v205
	s_nop 1
	v_permlane16_swap_b32_e32 v205, v206
	v_max_f32_e32 v206, v206, v206
	v_max_f32_e32 v205, v205, v205
	v_max_f32_e32 v205, v205, v206
	v_mov_b32_e32 v206, v205
	s_nop 1
	v_permlane32_swap_b32_e32 v205, v206
	v_max_f32_e32 v206, v206, v206
	v_max_f32_e32 v205, v205, v205
	v_max_f32_e32 v205, v205, v206
	v_cmp_gt_f32_e32 vcc, v205, v178
	s_cbranch_vccz .LBB0_813
	v_max_f32_e32 v205, v205, v205
	v_max_f32_e32 v206, v178, v178
	v_max_f32_e32 v205, v206, v205
	v_sub_f32_e32 v178, v178, v205
	v_exp_f32_e32 v178, v178
	s_nop 0
	v_mul_f32_e32 v188, v188, v178
	v_pk_mul_f32 v[36:37], v[36:37], v[178:179] op_sel_hi:[1,0]
	v_pk_mul_f32 v[34:35], v[34:35], v[178:179] op_sel_hi:[1,0]
	v_pk_mul_f32 v[32:33], v[32:33], v[178:179] op_sel_hi:[1,0]
	v_pk_mul_f32 v[30:31], v[30:31], v[178:179] op_sel_hi:[1,0]
	v_pk_mul_f32 v[28:29], v[28:29], v[178:179] op_sel_hi:[1,0]
	v_pk_mul_f32 v[26:27], v[26:27], v[178:179] op_sel_hi:[1,0]
	v_pk_mul_f32 v[24:25], v[24:25], v[178:179] op_sel_hi:[1,0]
	v_pk_mul_f32 v[22:23], v[22:23], v[178:179] op_sel_hi:[1,0]
	v_mov_b32_e32 v178, v205
.LBB0_813:
	v_sub_f32_e32 v138, v138, v178
	v_sub_f32_e32 v139, v139, v178
	v_sub_f32_e32 v140, v140, v178
	v_sub_f32_e32 v141, v141, v178
	v_sub_f32_e32 v134, v134, v178
	v_sub_f32_e32 v135, v135, v178
	v_sub_f32_e32 v136, v136, v178
	v_sub_f32_e32 v137, v137, v178
	v_exp_f32_e32 v138, v138
	v_exp_f32_e32 v139, v139
	v_exp_f32_e32 v140, v140
	v_exp_f32_e32 v141, v141
	v_exp_f32_e32 v134, v134
	v_exp_f32_e32 v135, v135
	v_exp_f32_e32 v136, v136
	v_exp_f32_e32 v137, v137
	v_cvt_pk_bf16_f32 v206, v138, v139
	v_cvt_pk_bf16_f32 v207, v140, v141
	v_cvt_pk_bf16_f32 v208, v134, v135
	v_cvt_pk_bf16_f32 v209, v136, v137
	s_nop 1
	v_mfma_f32_16x16x32_bf16 v[34:37], v[114:117], v[206:209], v[34:37]
	v_mfma_f32_16x16x32_bf16 v[30:33], v[102:105], v[206:209], v[30:33]
	v_mfma_f32_16x16x32_bf16 v[26:29], v[98:101], v[206:209], v[26:29]
	v_mfma_f32_16x16x32_bf16 v[22:25], v[86:89], v[206:209], v[22:25]
	s_waitcnt lgkmcnt(0)
	v_mfma_f32_16x16x32_fp8_fp8 v[206:209], v[130:131], v[82:83], v[238:241]
	v_mfma_f32_16x16x32_fp8_fp8 v[210:213], v[126:127], v[82:83], v[242:245]
	v_mfma_f32_16x16x32_fp8_fp8 v[130:133], v[132:133], v[84:85], v[206:209]
	v_mfma_f32_16x16x32_fp8_fp8 v[126:129], v[128:129], v[84:85], v[210:213]
	s_nop 6
	v_max_f32_e32 v205, v131, v131
	v_max_f32_e32 v206, v130, v130
	v_max_f32_e32 v207, v133, v133
	v_max_f32_e32 v205, v206, v205
	v_max_f32_e32 v206, v132, v132
	v_max_f32_e32 v206, v206, v207
	v_max_f32_e32 v207, v129, v129
	v_max_f32_e32 v208, v128, v128
	v_max_f32_e32 v207, v208, v207
	v_max3_f32 v207, v126, v127, v207
	v_max3_f32 v205, v205, v206, v207
	v_mov_b32_e32 v206, v205
	s_nop 1
	v_permlane16_swap_b32_e32 v205, v206
	v_max_f32_e32 v206, v206, v206
	v_max_f32_e32 v205, v205, v205
	v_max_f32_e32 v205, v205, v206
	v_mov_b32_e32 v206, v205
	s_nop 1
	v_permlane32_swap_b32_e32 v205, v206
	v_max_f32_e32 v206, v206, v206
	v_max_f32_e32 v205, v205, v205
	v_max_f32_e32 v205, v205, v206
	v_cmp_gt_f32_e32 vcc, v205, v179
	s_cbranch_vccz .LBB0_815
	v_max_f32_e32 v205, v205, v205
	v_max_f32_e32 v206, v179, v179
	v_max_f32_e32 v205, v206, v205
	v_sub_f32_e32 v179, v179, v205
	v_exp_f32_e32 v206, v179
	v_mov_b32_e32 v179, v205
	v_mul_f32_e32 v187, v187, v206
	v_pk_mul_f32 v[20:21], v[20:21], v[206:207] op_sel_hi:[1,0]
	v_pk_mul_f32 v[18:19], v[18:19], v[206:207] op_sel_hi:[1,0]
	v_pk_mul_f32 v[16:17], v[16:17], v[206:207] op_sel_hi:[1,0]
	v_pk_mul_f32 v[14:15], v[14:15], v[206:207] op_sel_hi:[1,0]
	v_pk_mul_f32 v[12:13], v[12:13], v[206:207] op_sel_hi:[1,0]
	v_pk_mul_f32 v[10:11], v[10:11], v[206:207] op_sel_hi:[1,0]
	v_pk_mul_f32 v[8:9], v[8:9], v[206:207] op_sel_hi:[1,0]
	v_pk_mul_f32 v[6:7], v[6:7], v[206:207] op_sel_hi:[1,0]
